# pooling mixer: the serial per-lane warm-up loop (up to 15 dependent row loads) replaced by 15 masked loads in flight and one wait; sums added in the same order
# speedup vs baseline: 1.0050x; 1.0050x over previous
.LBB0_1044:
	v_ashrrev_i32_e32 v79, 2, v1
	v_and_b32_e32 v58, 0xffffffe0, v79
	v_ashrrev_i32_e32 v59, 31, v58
	v_lshlrev_b32_e32 v2, 1, v76
	v_lshlrev_b32_e32 v3, 3, v1
	v_lshlrev_b64 v[12:13], 11, v[58:59]
	s_movk_i32 s6, 0x7f0
	v_and_b32_e32 v4, 0x3f8, v3
	v_bfe_u32 v3, v3, 8, 2
	v_and_or_b32 v2, v2, s6, v12
	v_readlane_b32 s6, v242, 28
	v_lshlrev_b32_e64 v77, v3, 2
	v_mov_b32_e32 v3, v13
	v_readlane_b32 s7, v242, 29
	v_mov_b32_e32 v50, 0
	s_mov_b32 s10, 1
	v_and_b32_e32 v78, 0xfe0, v79
	v_lshl_add_u64 v[2:3], s[6:7], 0, v[2:3]
	s_mov_b64 s[6:7], 0
	v_mov_b32_e32 v51, v50
	v_mov_b32_e32 v66, v50
	v_mov_b32_e32 v67, v50
	v_mov_b32_e32 v42, v50
	v_mov_b32_e32 v43, v50
	v_mov_b32_e32 v44, v50
	v_mov_b32_e32 v45, v50
	v_mov_b32_e32 v90, 0
	v_mov_b32_e32 v91, 0
	v_mov_b32_e32 v92, 0
	v_mov_b32_e32 v93, 0
	v_mov_b32_e32 v94, 0
	v_mov_b32_e32 v95, 0
	v_mov_b32_e32 v96, 0
	v_mov_b32_e32 v97, 0
	v_mov_b32_e32 v98, 0
	v_mov_b32_e32 v99, 0
	v_mov_b32_e32 v100, 0
	v_mov_b32_e32 v101, 0
	v_mov_b32_e32 v102, 0
	v_mov_b32_e32 v103, 0
	v_mov_b32_e32 v104, 0
	v_mov_b32_e32 v105, 0
	v_mov_b32_e32 v106, 0
	v_mov_b32_e32 v107, 0
	v_mov_b32_e32 v108, 0
	v_mov_b32_e32 v109, 0
	v_mov_b32_e32 v110, 0
	v_mov_b32_e32 v111, 0
	v_mov_b32_e32 v112, 0
	v_mov_b32_e32 v113, 0
	v_mov_b32_e32 v114, 0
	v_mov_b32_e32 v115, 0
	v_mov_b32_e32 v116, 0
	v_mov_b32_e32 v117, 0
	v_mov_b32_e32 v118, 0
	v_mov_b32_e32 v119, 0
	v_mov_b32_e32 v120, 0
	v_mov_b32_e32 v121, 0
	v_mov_b32_e32 v122, 0
	v_mov_b32_e32 v123, 0
	v_mov_b32_e32 v124, 0
	v_mov_b32_e32 v125, 0
	v_mov_b32_e32 v126, 0
	v_mov_b32_e32 v127, 0
	v_mov_b32_e32 v128, 0
	v_mov_b32_e32 v129, 0
	v_mov_b32_e32 v130, 0
	v_mov_b32_e32 v131, 0
	v_mov_b32_e32 v132, 0
	v_mov_b32_e32 v133, 0
	v_mov_b32_e32 v134, 0
	v_mov_b32_e32 v135, 0
	v_mov_b32_e32 v136, 0
	v_mov_b32_e32 v137, 0
	v_mov_b32_e32 v138, 0
	v_mov_b32_e32 v139, 0
	v_mov_b32_e32 v140, 0
	v_mov_b32_e32 v141, 0
	v_mov_b32_e32 v142, 0
	v_mov_b32_e32 v143, 0
	v_mov_b32_e32 v144, 0
	v_mov_b32_e32 v145, 0
	v_mov_b32_e32 v146, 0
	v_mov_b32_e32 v147, 0
	v_mov_b32_e32 v148, 0
	v_mov_b32_e32 v149, 0
	s_mov_b32 s6, 0xfffff800
	s_mov_b32 s7, -1
	v_cmp_lt_u32_e64 s[8:9], 1, v77
	v_cmp_le_u32_e32 vcc, 1, v78
	s_and_b64 vcc, vcc, s[8:9]
	s_and_saveexec_b64 s[8:9], vcc
	global_load_dwordx4 v[90:93], v[2:3], off
	s_or_b64 exec, exec, s[8:9]
	v_lshl_add_u64 v[2:3], v[2:3], 0, s[6:7]
	v_cmp_lt_u32_e64 s[8:9], 2, v77
	v_cmp_le_u32_e32 vcc, 2, v78
	s_and_b64 vcc, vcc, s[8:9]
	s_and_saveexec_b64 s[8:9], vcc
	global_load_dwordx4 v[94:97], v[2:3], off
	s_or_b64 exec, exec, s[8:9]
	v_lshl_add_u64 v[2:3], v[2:3], 0, s[6:7]
	v_cmp_lt_u32_e64 s[8:9], 3, v77
	v_cmp_le_u32_e32 vcc, 3, v78
	s_and_b64 vcc, vcc, s[8:9]
	s_and_saveexec_b64 s[8:9], vcc
	global_load_dwordx4 v[98:101], v[2:3], off
	s_or_b64 exec, exec, s[8:9]
	v_lshl_add_u64 v[2:3], v[2:3], 0, s[6:7]
	v_cmp_lt_u32_e64 s[8:9], 4, v77
	v_cmp_le_u32_e32 vcc, 4, v78
	s_and_b64 vcc, vcc, s[8:9]
	s_and_saveexec_b64 s[8:9], vcc
	global_load_dwordx4 v[102:105], v[2:3], off
	s_or_b64 exec, exec, s[8:9]
	v_lshl_add_u64 v[2:3], v[2:3], 0, s[6:7]
	v_cmp_lt_u32_e64 s[8:9], 5, v77
	v_cmp_le_u32_e32 vcc, 5, v78
	s_and_b64 vcc, vcc, s[8:9]
	s_and_saveexec_b64 s[8:9], vcc
	global_load_dwordx4 v[106:109], v[2:3], off
	s_or_b64 exec, exec, s[8:9]
	v_lshl_add_u64 v[2:3], v[2:3], 0, s[6:7]
	v_cmp_lt_u32_e64 s[8:9], 6, v77
	v_cmp_le_u32_e32 vcc, 6, v78
	s_and_b64 vcc, vcc, s[8:9]
	s_and_saveexec_b64 s[8:9], vcc
	global_load_dwordx4 v[110:113], v[2:3], off
	s_or_b64 exec, exec, s[8:9]
	v_lshl_add_u64 v[2:3], v[2:3], 0, s[6:7]
	v_cmp_lt_u32_e64 s[8:9], 7, v77
	v_cmp_le_u32_e32 vcc, 7, v78
	s_and_b64 vcc, vcc, s[8:9]
	s_and_saveexec_b64 s[8:9], vcc
	global_load_dwordx4 v[114:117], v[2:3], off
	s_or_b64 exec, exec, s[8:9]
	v_lshl_add_u64 v[2:3], v[2:3], 0, s[6:7]
	v_cmp_lt_u32_e64 s[8:9], 8, v77
	v_cmp_le_u32_e32 vcc, 8, v78
	s_and_b64 vcc, vcc, s[8:9]
	s_and_saveexec_b64 s[8:9], vcc
	global_load_dwordx4 v[118:121], v[2:3], off
	s_or_b64 exec, exec, s[8:9]
	v_lshl_add_u64 v[2:3], v[2:3], 0, s[6:7]
	v_cmp_lt_u32_e64 s[8:9], 9, v77
	v_cmp_le_u32_e32 vcc, 9, v78
	s_and_b64 vcc, vcc, s[8:9]
	s_and_saveexec_b64 s[8:9], vcc
	global_load_dwordx4 v[122:125], v[2:3], off
	s_or_b64 exec, exec, s[8:9]
	v_lshl_add_u64 v[2:3], v[2:3], 0, s[6:7]
	v_cmp_lt_u32_e64 s[8:9], 10, v77
	v_cmp_le_u32_e32 vcc, 10, v78
	s_and_b64 vcc, vcc, s[8:9]
	s_and_saveexec_b64 s[8:9], vcc
	global_load_dwordx4 v[126:129], v[2:3], off
	s_or_b64 exec, exec, s[8:9]
	v_lshl_add_u64 v[2:3], v[2:3], 0, s[6:7]
	v_cmp_lt_u32_e64 s[8:9], 11, v77
	v_cmp_le_u32_e32 vcc, 11, v78
	s_and_b64 vcc, vcc, s[8:9]
	s_and_saveexec_b64 s[8:9], vcc
	global_load_dwordx4 v[130:133], v[2:3], off
	s_or_b64 exec, exec, s[8:9]
	v_lshl_add_u64 v[2:3], v[2:3], 0, s[6:7]
	v_cmp_lt_u32_e64 s[8:9], 12, v77
	v_cmp_le_u32_e32 vcc, 12, v78
	s_and_b64 vcc, vcc, s[8:9]
	s_and_saveexec_b64 s[8:9], vcc
	global_load_dwordx4 v[134:137], v[2:3], off
	s_or_b64 exec, exec, s[8:9]
	v_lshl_add_u64 v[2:3], v[2:3], 0, s[6:7]
	v_cmp_lt_u32_e64 s[8:9], 13, v77
	v_cmp_le_u32_e32 vcc, 13, v78
	s_and_b64 vcc, vcc, s[8:9]
	s_and_saveexec_b64 s[8:9], vcc
	global_load_dwordx4 v[138:141], v[2:3], off
	s_or_b64 exec, exec, s[8:9]
	v_lshl_add_u64 v[2:3], v[2:3], 0, s[6:7]
	v_cmp_lt_u32_e64 s[8:9], 14, v77
	v_cmp_le_u32_e32 vcc, 14, v78
	s_and_b64 vcc, vcc, s[8:9]
	s_and_saveexec_b64 s[8:9], vcc
	global_load_dwordx4 v[142:145], v[2:3], off
	s_or_b64 exec, exec, s[8:9]
	v_lshl_add_u64 v[2:3], v[2:3], 0, s[6:7]
	v_cmp_lt_u32_e64 s[8:9], 15, v77
	v_cmp_le_u32_e32 vcc, 15, v78
	s_and_b64 vcc, vcc, s[8:9]
	s_and_saveexec_b64 s[8:9], vcc
	global_load_dwordx4 v[146:149], v[2:3], off
	s_or_b64 exec, exec, s[8:9]
	v_lshl_add_u64 v[2:3], v[2:3], 0, s[6:7]
	s_waitcnt vmcnt(0)
	v_lshlrev_b32_e32 v10, 16, v90
	v_and_b32_e32 v11, 0xffff0000, v90
	v_lshlrev_b32_e32 v6, 16, v91
	v_and_b32_e32 v7, 0xffff0000, v91
	v_pk_add_f32 v[66:67], v[66:67], v[6:7]
	v_lshlrev_b32_e32 v6, 16, v92
	v_and_b32_e32 v7, 0xffff0000, v92
	v_pk_add_f32 v[42:43], v[42:43], v[6:7]
	v_lshlrev_b32_e32 v6, 16, v93
	v_and_b32_e32 v7, 0xffff0000, v93
	v_pk_add_f32 v[50:51], v[50:51], v[10:11]
	v_pk_add_f32 v[44:45], v[44:45], v[6:7]
	v_lshlrev_b32_e32 v10, 16, v94
	v_and_b32_e32 v11, 0xffff0000, v94
	v_lshlrev_b32_e32 v6, 16, v95
	v_and_b32_e32 v7, 0xffff0000, v95
	v_pk_add_f32 v[66:67], v[66:67], v[6:7]
	v_lshlrev_b32_e32 v6, 16, v96
	v_and_b32_e32 v7, 0xffff0000, v96
	v_pk_add_f32 v[42:43], v[42:43], v[6:7]
	v_lshlrev_b32_e32 v6, 16, v97
	v_and_b32_e32 v7, 0xffff0000, v97
	v_pk_add_f32 v[50:51], v[50:51], v[10:11]
	v_pk_add_f32 v[44:45], v[44:45], v[6:7]
	v_lshlrev_b32_e32 v10, 16, v98
	v_and_b32_e32 v11, 0xffff0000, v98
	v_lshlrev_b32_e32 v6, 16, v99
	v_and_b32_e32 v7, 0xffff0000, v99
	v_pk_add_f32 v[66:67], v[66:67], v[6:7]
	v_lshlrev_b32_e32 v6, 16, v100
	v_and_b32_e32 v7, 0xffff0000, v100
	v_pk_add_f32 v[42:43], v[42:43], v[6:7]
	v_lshlrev_b32_e32 v6, 16, v101
	v_and_b32_e32 v7, 0xffff0000, v101
	v_pk_add_f32 v[50:51], v[50:51], v[10:11]
	v_pk_add_f32 v[44:45], v[44:45], v[6:7]
	v_lshlrev_b32_e32 v10, 16, v102
	v_and_b32_e32 v11, 0xffff0000, v102
	v_lshlrev_b32_e32 v6, 16, v103
	v_and_b32_e32 v7, 0xffff0000, v103
	v_pk_add_f32 v[66:67], v[66:67], v[6:7]
	v_lshlrev_b32_e32 v6, 16, v104
	v_and_b32_e32 v7, 0xffff0000, v104
	v_pk_add_f32 v[42:43], v[42:43], v[6:7]
	v_lshlrev_b32_e32 v6, 16, v105
	v_and_b32_e32 v7, 0xffff0000, v105
	v_pk_add_f32 v[50:51], v[50:51], v[10:11]
	v_pk_add_f32 v[44:45], v[44:45], v[6:7]
	v_lshlrev_b32_e32 v10, 16, v106
	v_and_b32_e32 v11, 0xffff0000, v106
	v_lshlrev_b32_e32 v6, 16, v107
	v_and_b32_e32 v7, 0xffff0000, v107
	v_pk_add_f32 v[66:67], v[66:67], v[6:7]
	v_lshlrev_b32_e32 v6, 16, v108
	v_and_b32_e32 v7, 0xffff0000, v108
	v_pk_add_f32 v[42:43], v[42:43], v[6:7]
	v_lshlrev_b32_e32 v6, 16, v109
	v_and_b32_e32 v7, 0xffff0000, v109
	v_pk_add_f32 v[50:51], v[50:51], v[10:11]
	v_pk_add_f32 v[44:45], v[44:45], v[6:7]
	v_lshlrev_b32_e32 v10, 16, v110
	v_and_b32_e32 v11, 0xffff0000, v110
	v_lshlrev_b32_e32 v6, 16, v111
	v_and_b32_e32 v7, 0xffff0000, v111
	v_pk_add_f32 v[66:67], v[66:67], v[6:7]
	v_lshlrev_b32_e32 v6, 16, v112
	v_and_b32_e32 v7, 0xffff0000, v112
	v_pk_add_f32 v[42:43], v[42:43], v[6:7]
	v_lshlrev_b32_e32 v6, 16, v113
	v_and_b32_e32 v7, 0xffff0000, v113
	v_pk_add_f32 v[50:51], v[50:51], v[10:11]
	v_pk_add_f32 v[44:45], v[44:45], v[6:7]
	v_lshlrev_b32_e32 v10, 16, v114
	v_and_b32_e32 v11, 0xffff0000, v114
	v_lshlrev_b32_e32 v6, 16, v115
	v_and_b32_e32 v7, 0xffff0000, v115
	v_pk_add_f32 v[66:67], v[66:67], v[6:7]
	v_lshlrev_b32_e32 v6, 16, v116
	v_and_b32_e32 v7, 0xffff0000, v116
	v_pk_add_f32 v[42:43], v[42:43], v[6:7]
	v_lshlrev_b32_e32 v6, 16, v117
	v_and_b32_e32 v7, 0xffff0000, v117
	v_pk_add_f32 v[50:51], v[50:51], v[10:11]
	v_pk_add_f32 v[44:45], v[44:45], v[6:7]
	v_lshlrev_b32_e32 v10, 16, v118
	v_and_b32_e32 v11, 0xffff0000, v118
	v_lshlrev_b32_e32 v6, 16, v119
	v_and_b32_e32 v7, 0xffff0000, v119
	v_pk_add_f32 v[66:67], v[66:67], v[6:7]
	v_lshlrev_b32_e32 v6, 16, v120
	v_and_b32_e32 v7, 0xffff0000, v120
	v_pk_add_f32 v[42:43], v[42:43], v[6:7]
	v_lshlrev_b32_e32 v6, 16, v121
	v_and_b32_e32 v7, 0xffff0000, v121
	v_pk_add_f32 v[50:51], v[50:51], v[10:11]
	v_pk_add_f32 v[44:45], v[44:45], v[6:7]
	v_lshlrev_b32_e32 v10, 16, v122
	v_and_b32_e32 v11, 0xffff0000, v122
	v_lshlrev_b32_e32 v6, 16, v123
	v_and_b32_e32 v7, 0xffff0000, v123
	v_pk_add_f32 v[66:67], v[66:67], v[6:7]
	v_lshlrev_b32_e32 v6, 16, v124
	v_and_b32_e32 v7, 0xffff0000, v124
	v_pk_add_f32 v[42:43], v[42:43], v[6:7]
	v_lshlrev_b32_e32 v6, 16, v125
	v_and_b32_e32 v7, 0xffff0000, v125
	v_pk_add_f32 v[50:51], v[50:51], v[10:11]
	v_pk_add_f32 v[44:45], v[44:45], v[6:7]
	v_lshlrev_b32_e32 v10, 16, v126
	v_and_b32_e32 v11, 0xffff0000, v126
	v_lshlrev_b32_e32 v6, 16, v127
	v_and_b32_e32 v7, 0xffff0000, v127
	v_pk_add_f32 v[66:67], v[66:67], v[6:7]
	v_lshlrev_b32_e32 v6, 16, v128
	v_and_b32_e32 v7, 0xffff0000, v128
	v_pk_add_f32 v[42:43], v[42:43], v[6:7]
	v_lshlrev_b32_e32 v6, 16, v129
	v_and_b32_e32 v7, 0xffff0000, v129
	v_pk_add_f32 v[50:51], v[50:51], v[10:11]
	v_pk_add_f32 v[44:45], v[44:45], v[6:7]
	v_lshlrev_b32_e32 v10, 16, v130
	v_and_b32_e32 v11, 0xffff0000, v130
	v_lshlrev_b32_e32 v6, 16, v131
	v_and_b32_e32 v7, 0xffff0000, v131
	v_pk_add_f32 v[66:67], v[66:67], v[6:7]
	v_lshlrev_b32_e32 v6, 16, v132
	v_and_b32_e32 v7, 0xffff0000, v132
	v_pk_add_f32 v[42:43], v[42:43], v[6:7]
	v_lshlrev_b32_e32 v6, 16, v133
	v_and_b32_e32 v7, 0xffff0000, v133
	v_pk_add_f32 v[50:51], v[50:51], v[10:11]
	v_pk_add_f32 v[44:45], v[44:45], v[6:7]
	v_lshlrev_b32_e32 v10, 16, v134
	v_and_b32_e32 v11, 0xffff0000, v134
	v_lshlrev_b32_e32 v6, 16, v135
	v_and_b32_e32 v7, 0xffff0000, v135
	v_pk_add_f32 v[66:67], v[66:67], v[6:7]
	v_lshlrev_b32_e32 v6, 16, v136
	v_and_b32_e32 v7, 0xffff0000, v136
	v_pk_add_f32 v[42:43], v[42:43], v[6:7]
	v_lshlrev_b32_e32 v6, 16, v137
	v_and_b32_e32 v7, 0xffff0000, v137
	v_pk_add_f32 v[50:51], v[50:51], v[10:11]
	v_pk_add_f32 v[44:45], v[44:45], v[6:7]
	v_lshlrev_b32_e32 v10, 16, v138
	v_and_b32_e32 v11, 0xffff0000, v138
	v_lshlrev_b32_e32 v6, 16, v139
	v_and_b32_e32 v7, 0xffff0000, v139
	v_pk_add_f32 v[66:67], v[66:67], v[6:7]
	v_lshlrev_b32_e32 v6, 16, v140
	v_and_b32_e32 v7, 0xffff0000, v140
	v_pk_add_f32 v[42:43], v[42:43], v[6:7]
	v_lshlrev_b32_e32 v6, 16, v141
	v_and_b32_e32 v7, 0xffff0000, v141
	v_pk_add_f32 v[50:51], v[50:51], v[10:11]
	v_pk_add_f32 v[44:45], v[44:45], v[6:7]
	v_lshlrev_b32_e32 v10, 16, v142
	v_and_b32_e32 v11, 0xffff0000, v142
	v_lshlrev_b32_e32 v6, 16, v143
	v_and_b32_e32 v7, 0xffff0000, v143
	v_pk_add_f32 v[66:67], v[66:67], v[6:7]
	v_lshlrev_b32_e32 v6, 16, v144
	v_and_b32_e32 v7, 0xffff0000, v144
	v_pk_add_f32 v[42:43], v[42:43], v[6:7]
	v_lshlrev_b32_e32 v6, 16, v145
	v_and_b32_e32 v7, 0xffff0000, v145
	v_pk_add_f32 v[50:51], v[50:51], v[10:11]
	v_pk_add_f32 v[44:45], v[44:45], v[6:7]
	v_lshlrev_b32_e32 v10, 16, v146
	v_and_b32_e32 v11, 0xffff0000, v146
	v_lshlrev_b32_e32 v6, 16, v147
	v_and_b32_e32 v7, 0xffff0000, v147
	v_pk_add_f32 v[66:67], v[66:67], v[6:7]
	v_lshlrev_b32_e32 v6, 16, v148
	v_and_b32_e32 v7, 0xffff0000, v148
	v_pk_add_f32 v[42:43], v[42:43], v[6:7]
	v_lshlrev_b32_e32 v6, 16, v149
	v_and_b32_e32 v7, 0xffff0000, v149
	v_pk_add_f32 v[50:51], v[50:51], v[10:11]
	v_pk_add_f32 v[44:45], v[44:45], v[6:7]
	s_mov_b64 s[6:7], exec
